# next dilated unit's Q rows and first three K/V tiles requested before the current unit's epilogue
# baseline (speedup 1.0000x reference)
; __device__ __forceinline__ void dil_unit(Frame& F, const AttnBufs& A, int b, int h, int g, int r, int c) {
;     char* shm = (char*)F.lds; const int tid = F.tid, lane = tid & 63, r32 = lane & 31, hi = lane >> 5, w = F.wave;
;     const int dil = (g == 0) ? 1 : (g == 1 ? 4 : 16);
;     const int i0 = 256 * c;
;     att::BiasDil B; B.sd = exp2f(-8.0f * (float)(h - 10 + 1) / 10.0f) * LOG2E * (float)dil; B.qrel = 128 + w * 32 + r32; B.hi = hi; B.w = w; B.setup(r32);
;     const long tok_q0 = (long)b * SEQ + r + (long)dil * (i0 + w * 32);
;     const long tok_k0 = (long)b * SEQ + r + (long)dil * (i0 - 128);
;     const long bo = (long)b * (long)BADJ;
;     att::UnitIO io; io.Q = A.Q + bo + tok_q0 * DM + h * 64; io.qstride = (long)DM * dil; io.K0 = A.K + bo + tok_k0 * DM + h * 64; io.V0 = A.V + bo + tok_k0 * DM + h * 64; io.kstride = (long)DM * dil;
; __device__ __forceinline__ void attn_phase(Frame& F, const AttnBufs& A) {
;     ...
;     for (int k = 0; k < 9; ++k) { const int idx = r + 32 * k, h6 = idx / 48, rest = idx % 48, br = rest >> 4, i16 = rest & 15;
;         const int rr = (br == 0) ? 0 : (br == 1 ? (i16 >> 2) : i16), c = (br == 0) ? i16 : (br == 1 ? (i16 & 3) : 0);
.LBB0_363:
	s_lshl_b32 s56, s74, 5
	v_readlane_b32 s2, v254, 30
	s_or_b32 s56, s56, s2
	s_mul_hi_u32 s57, s56, 0xaaaaaaab
	s_lshr_b32 s75, s57, 5
	s_mul_i32 s57, s75, 48
	s_sub_i32 s66, s56, s57
	s_lshr_b32 s2, s66, 4
	s_and_b32 s67, s66, 15
	s_cmp_lt_u32 s66, 16
	s_cselect_b64 s[62:63], -1, 0
	s_cmp_eq_u32 s2, 1
	s_cselect_b64 s[64:65], -1, 0
	s_bfe_u32 s68, s66, 0x20002
	s_and_b64 s[56:57], s[64:65], exec
	s_cselect_b32 s68, s68, s67
	s_and_b64 s[56:57], s[62:63], exec
	s_cselect_b32 s68, 0, s68
	s_and_b32 s66, s66, 3
	s_and_b64 s[56:57], s[64:65], exec
	s_cselect_b32 s66, s66, 0
	s_and_b64 s[56:57], s[62:63], exec
	s_cselect_b32 s76, s67, s66
	s_and_b64 s[56:57], s[64:65], exec
	s_cselect_b32 s66, 4, 16
	s_and_b64 s[56:57], s[62:63], exec
	s_cselect_b32 s80, 1, s66
	s_not_b32 s56, s75
	s_lshl_b32 s56, s56, 3
	v_cvt_f32_i32_e32 v0, s56
	s_mov_b32 s84, 0x41200000
	s_mov_b32 s85, 0x41300000
	s_lshl_b32 s69, s76, 8
	v_div_scale_f32 v2, s[56:57], s84, s84, v0
	v_rcp_f32_e32 v3, v2
	s_mov_b32 s56, 0xc2fc0000
	v_readlane_b32 s70, v254, 38
	v_readlane_b32 s71, v254, 39
	v_fma_f32 v4, -v2, v3, 1.0
	v_fmac_f32_e32 v3, v4, v3
	v_div_scale_f32 v4, vcc, v0, s84, v0
	v_mul_f32_e32 v5, v4, v3
	v_fma_f32 v6, -v2, v5, v4
	v_fmac_f32_e32 v5, v6, v3
	v_fma_f32 v2, -v2, v5, v4
	v_div_fmas_f32 v2, v2, v3, v5
	v_div_fixup_f32 v0, v2, s84, v0
	v_cmp_gt_f32_e32 vcc, s56, v0
	s_and_b64 s[56:57], vcc, exec
	v_readlane_b32 s56, v254, 48
	s_cselect_b32 s81, 0xffffffc0, 0
	s_add_i32 s56, s69, s56
	s_or_b32 s68, s70, s68
	s_ashr_i32 s57, s56, 31
	s_and_b64 s[66:67], s[64:65], exec
	s_cselect_b32 s70, 2, 4
	s_and_b64 s[66:67], s[62:63], exec
	s_cselect_b32 s70, 0, s70
	s_lshl_b64 s[56:57], s[56:57], s70
	s_add_u32 s66, s56, s68
	s_addc_u32 s67, s57, s71
	s_add_i32 s56, s69, 0xffffff80
	s_ashr_i32 s57, s56, 31
	s_lshl_b64 s[56:57], s[56:57], s70
	s_add_u32 s56, s56, s68
	s_addc_u32 s57, s57, s71
	s_lshl_b64 s[68:69], s[66:67], 11
	v_readlane_b32 s70, v254, 42
	s_add_u32 s68, s70, s68
	v_readlane_b32 s70, v254, 45
	s_addc_u32 s69, s70, s69
	s_lshl_b32 s70, s75, 6
	s_lshl_b32 s77, s75, 7
	v_writelane_b32 v255, s70, 49
	s_add_u32 s70, s68, s77
	s_addc_u32 s71, s69, 0
	s_lshl_b64 s[68:69], s[56:57], 11
	v_readlane_b32 s56, v254, 49
	s_add_u32 s56, s56, s68
	v_readlane_b32 s57, v254, 50
	s_addc_u32 s57, s57, s69
	s_add_u32 s56, s56, s77
	s_addc_u32 s57, s57, 0
	v_readlane_b32 s78, v254, 53
	s_add_u32 s68, s78, s68
	v_readlane_b32 s78, v254, 54
	s_addc_u32 s69, s78, s69
	s_add_u32 s68, s68, s77
	s_addc_u32 s69, s69, 0
	s_cmp_eq_u32 s76, 0
	v_readfirstlane_b32 s77, v232
	s_cselect_b32 s88, 2, 0
	s_ashr_i32 s76, s77, 6
	s_and_b64 s[78:79], s[64:65], exec
	s_cselect_b32 s82, 12, 14
	s_and_b64 s[78:79], s[62:63], exec
	s_cselect_b32 s83, 10, s82
	v_lshlrev_b64 v[2:3], s83, v[146:147]
	v_lshl_add_u64 v[2:3], v[2:3], 1, s[70:71]
	v_mov_b32_e32 v149, v1
	v_lshl_add_u64 v[2:3], v[2:3], 0, v[148:149]
	s_cmp_lg_u32 s74, 0
	s_cbranch_scc1 .Ldil_skq
	flat_load_dwordx4 v[98:101], v[2:3] offset:1280
	flat_load_dwordx4 v[102:105], v[2:3] offset:1312
	flat_load_dwordx4 v[106:109], v[2:3] offset:1344
	flat_load_dwordx4 v[110:113], v[2:3] offset:1376
; #define ATT_WAIT_BAR(N) asm volatile("s_waitcnt vmcnt(" #N ") lgkmcnt(0)\n\ts_barrier" ::: "memory")
; #define ATT_DMA(t, slot) do { glds16(ksrc + (long)(t) * tstep, (unsigned)__builtin_amdgcn_readfirstlane(kdst + (slot))); glds16(vsrc + (long)(t) * tstep, (unsigned)__builtin_amdgcn_readfirstlane(vdst + (slot))); } while (0)
; #pragma unroll
;         for (int i = 0; i < 8; ++i) { const int r = 2 * i; kc[i] = (f32x2_t){sd * (float)((r & 3) + 8 * (r >> 2)), sd * (float)(((r + 1) & 3) + 8 * ((r + 1) >> 2))}; } }
; template <class BIAS>
; __device__ __forceinline__ void attn_tiles(char* shm, const UnitIO& io, int t_begin, int t_end, const BIAS& B, int tid) {
;     const int lane = tid & 63, r32 = lane & 31, hi = lane >> 5; const int wid = __builtin_amdgcn_readfirstlane(tid >> 6);
;     const unsigned lds0 = (unsigned)(uintptr_t)shm;
;     const bf16* ksrc = io.K0 + (long)lane * io.kstride + wid * 8;
;     const bf16* vsrc = io.V0 + (long)(16 * (wid & 3) + (lane >> 2)) * io.kstride + (wid >> 2) * 32 + (lane & 3) * 8;
;     const unsigned kdst = lds0 + LDS_K + wid * 1024, vdst = lds0 + LDS_V + wid * 1024;
;     const long tstep = 64 * io.kstride;
;     ...
;     const lds_cptr shm3 = (lds_cptr)shm;
;     const lds_cptr kp0 = shm3 + LDS_K + hi * 1024 + r32 * 16;
;     const lds_cptr vp0 = shm3 + LDS_V + ((lane >> 4) & 1) * 32 + (lane & 3) * 8 + (4 * hi + ((lane & 15) >> 2)) * 64;
;     float* wsf = (float*)(shm + LDS_WS) + wid * 64;
;     bf16x8 qr[4];
;     { const bf16* qp = io.Q + (long)r32 * io.qstride + hi * 8;
; #pragma unroll
;       for (int d0 = 0; d0 < 4; ++d0) qr[d0] = *reinterpret_cast<const bf16x8*>(qp + d0 * 16); }
;     ATT_DMA(t_begin, 0);
;     asm volatile("" :: "v"(qr[0]), "v"(qr[1]), "v"(qr[2]), "v"(qr[3]));
;     const int nt_ = t_end - t_begin; if (nt_ > 1) ATT_DMA(t_begin + 1, SLOTB); if (nt_ > 2) ATT_DMA(t_begin + 2, 2 * SLOTB);
;     f32x16 o[2]; o[0] = f32x16{}; o[1] = f32x16{}; float l_reg = 0.f;
;     if (nt_ > 2) ATT_WAIT_BAR(4); else if (nt_ > 1) ATT_WAIT_BAR(2); else ATT_WAIT_BAR(0);
.Ldil_skq:
	v_cndmask_b32_e32 v4, 0, v224, vcc
	v_add_f32_e32 v0, v0, v4
	v_exp_f32_e32 v0, v0
	v_cvt_f32_ubyte0_e32 v3, s80
	s_mov_b32 s78, 2.0
	s_mov_b32 s79, 0x40400000
	v_ldexp_f32 v0, v0, s81
	v_mul_f32_e32 v0, 0x3fb8aa3b, v0
	v_mul_f32_e32 v155, v0, v3
	v_mov_b32_e32 v0, v155
	v_pk_mul_f32 v[158:159], v[0:1], s[78:79] op_sel_hi:[0,1]
	s_mov_b32 s78, 0x41000000
	s_mov_b32 s79, 0x41100000
	v_pk_mul_f32 v[160:161], v[0:1], s[78:79] op_sel_hi:[0,1]
	s_mov_b32 s78, 0x41800000
	s_mov_b32 s79, 0x41880000
	v_pk_mul_f32 v[164:165], v[0:1], s[78:79] op_sel_hi:[0,1]
	s_mov_b32 s78, 0x41900000
	s_mov_b32 s79, 0x41980000
	v_pk_mul_f32 v[166:167], v[0:1], s[78:79] op_sel_hi:[0,1]
	s_mov_b32 s78, 0x41c00000
	s_mov_b32 s79, 0x41c80000
	v_pk_mul_f32 v[168:169], v[0:1], s[78:79] op_sel_hi:[0,1]
	s_mov_b32 s78, 0x41d00000
	s_mov_b32 s79, 0x41d80000
	v_pk_mul_f32 v[170:171], v[0:1], s[78:79] op_sel_hi:[0,1]
	s_lshl_b32 s70, s76, 4
	s_ashr_i32 s79, s77, 3
	v_pk_mul_f32 v[162:163], v[0:1], s[84:85] op_sel_hi:[0,1]
	s_lshl_b32 s80, s76, 3
	s_lshl_b32 s78, s76, 10
	v_and_or_b32 v0, s70, 48, v178
	s_and_b32 s82, s79, 0xffffffe0
	v_lshlrev_b64 v[4:5], s83, v[194:195]
	s_ashr_i32 s81, s80, 31
	s_add_i32 s79, s78, 0x8000
	v_lshlrev_b64 v[6:7], s83, v[0:1]
	s_ashr_i32 s83, s82, 31
	v_lshl_add_u64 v[4:5], v[4:5], 1, s[56:57]
	s_and_b64 s[56:57], s[64:65], exec
	v_lshl_add_u64 v[172:173], s[80:81], 1, v[4:5]
	v_lshl_add_u64 v[4:5], v[6:7], 1, s[68:69]
	s_cselect_b32 s68, 18, 20
	s_and_b64 s[56:57], s[62:63], exec
	s_mov_b32 s89, s3
	s_cselect_b32 s80, 16, s68
	s_mov_b32 s71, s3
	s_or_b32 s70, s88, 1
	s_lshl_b64 s[56:57], s[88:89], s80
	v_mov_b32_e32 v151, v1
	v_lshl_add_u64 v[4:5], s[82:83], 1, v[4:5]
	s_lshl_b64 s[68:69], s[70:71], s80
	s_lshl_b64 s[56:57], s[56:57], 1
	v_lshl_add_u64 v[174:175], v[4:5], 0, v[150:151]
	s_lshl_b64 s[68:69], s[68:69], 1
	v_lshl_add_u64 v[4:5], v[172:173], 0, s[56:57]
	s_mov_b64 s[70:71], 0x500
	v_lshl_add_u64 v[6:7], v[174:175], 0, s[56:57]
	v_lshl_add_u64 v[8:9], v[172:173], 0, s[68:69]
	v_lshl_add_u64 v[4:5], v[4:5], 0, s[70:71]
	s_cmp_lg_u32 s74, 0
	s_cbranch_scc1 .Ldil_skd0
	s_mov_b32 s56, m0
	s_mov_b32 m0, s78
	s_nop 0
	global_load_lds_dwordx4 v[4:5], off
	s_mov_b32 m0, s56
.Ldil_skd0:
	s_add_i32 s81, s78, 0x2000
	v_lshl_add_u64 v[6:7], v[6:7], 0, s[70:71]
	v_lshl_add_u64 v[8:9], v[8:9], 0, s[70:71]
	s_cmp_lg_u32 s74, 0
	s_cbranch_scc1 .Ldil_skd1
	s_mov_b32 s56, m0
	s_mov_b32 m0, s79
	s_nop 0
	global_load_lds_dwordx4 v[6:7], off
	s_mov_b32 m0, s56
.Ldil_skd1:
	s_waitcnt vmcnt(0) lgkmcnt(0)
	s_cmp_lg_u32 s74, 0
	s_cbranch_scc1 .Ldil_skd2
	s_mov_b32 s56, m0
	s_mov_b32 m0, s81
	s_nop 0
	global_load_lds_dwordx4 v[8:9], off
	s_mov_b32 m0, s56
.Ldil_skd2:
	v_lshl_add_u64 v[4:5], v[174:175], 0, s[68:69]
	v_lshl_add_u64 v[4:5], v[4:5], 0, s[70:71]
	s_add_i32 s56, s79, 0x2000
	s_cmp_lg_u32 s74, 0
	s_cbranch_scc1 .Ldil_skd3
	s_mov_b32 s57, m0
	s_mov_b32 m0, s56
	s_nop 0
	global_load_lds_dwordx4 v[4:5], off
	s_mov_b32 m0, s57
.Ldil_skd3:
	s_add_i32 s56, s88, 2
	v_writelane_b32 v254, s2, 9
	s_mov_b32 s57, s3
	s_lshl_b64 s[56:57], s[56:57], s80
	s_lshl_b64 s[56:57], s[56:57], 1
	v_lshl_add_u64 v[4:5], v[172:173], 0, s[56:57]
	v_lshl_add_u64 v[4:5], v[4:5], 0, s[70:71]
	s_add_i32 s68, s78, 0x4000
	s_cmp_lg_u32 s74, 0
	s_cbranch_scc1 .Ldil_skd4
	s_mov_b32 s69, m0
	s_mov_b32 m0, s68
	s_nop 0
	global_load_lds_dwordx4 v[4:5], off
	s_mov_b32 m0, s69
.Ldil_skd4:
	v_lshl_add_u64 v[4:5], v[174:175], 0, s[56:57]
	v_mov_b32_e32 v2, 0
	v_lshl_add_u64 v[4:5], v[4:5], 0, s[70:71]
	s_add_i32 s56, s79, 0x4000
	s_cmp_lg_u32 s74, 0
	s_cbranch_scc1 .Ldil_skd5
	s_mov_b32 s57, m0
	s_mov_b32 m0, s56
	s_nop 0
	global_load_lds_dwordx4 v[4:5], off
	s_mov_b32 m0, s57
.Ldil_skd5:
	s_waitcnt vmcnt(4) lgkmcnt(0)
	s_barrier
	v_mov_b32_e32 v16, v2
	v_mov_b32_e32 v17, v2
	v_mul_f32_e32 v156, 0x42000000, v155
	v_mov_b32_e32 v3, v2
	v_mov_b32_e32 v4, v2
	v_mov_b32_e32 v5, v2
	v_mov_b32_e32 v6, v2
	v_mov_b32_e32 v7, v2
	v_mov_b32_e32 v8, v2
	v_mov_b32_e32 v9, v2
	v_mov_b32_e32 v10, v2
	v_mov_b32_e32 v11, v2
	v_mov_b32_e32 v12, v2
	v_mov_b32_e32 v13, v2
	v_mov_b32_e32 v14, v2
	v_mov_b32_e32 v15, v2
	v_mov_b64_e32 v[32:33], v[16:17]
	v_mul_f32_e32 v149, 0x42800000, v155
	v_mul_f32_e32 v154, 0, v155
	v_writelane_b32 v254, s3, 10
	v_mul_f32_e32 v0, v155, v196
	v_mov_b32_e32 v176, v156
	v_mov_b32_e32 v177, v156
	s_movk_i32 s81, 0x6000
	v_mov_b64_e32 v[30:31], v[14:15]
	v_mov_b64_e32 v[28:29], v[12:13]
	v_mov_b64_e32 v[26:27], v[10:11]
	v_mov_b64_e32 v[24:25], v[8:9]
	v_mov_b64_e32 v[22:23], v[6:7]
	v_mov_b64_e32 v[20:21], v[4:5]
	v_mov_b64_e32 v[18:19], v[2:3]
	v_mov_b32_e32 v151, v2
	s_branch .LBB0_365

; #define ATT_WAIT_BAR(N) asm volatile("s_waitcnt vmcnt(" #N ") lgkmcnt(0)\n\ts_barrier" ::: "memory")
; #define ATT_DMA(t, slot) do { glds16(ksrc + (long)(t) * tstep, (unsigned)__builtin_amdgcn_readfirstlane(kdst + (slot))); glds16(vsrc + (long)(t) * tstep, (unsigned)__builtin_amdgcn_readfirstlane(vdst + (slot))); } while (0)
; template <class BIAS>
; __device__ __forceinline__ void attn_tiles(char* shm, const UnitIO& io, int t_begin, int t_end, const BIAS& B, int tid) {
;     ...
;     const lds_cptr shm3 = (lds_cptr)shm;
;     const lds_cptr kp0 = shm3 + LDS_K + hi * 1024 + r32 * 16;
;     const lds_cptr vp0 = shm3 + LDS_V + ((lane >> 4) & 1) * 32 + (lane & 3) * 8 + (4 * hi + ((lane & 15) >> 2)) * 64;
;     float* wsf = (float*)(shm + LDS_WS) + wid * 64;
;     bf16x8 qr[4];
;     { const bf16* qp = io.Q + (long)r32 * io.qstride + hi * 8;
; #pragma unroll
;       for (int d0 = 0; d0 < 4; ++d0) qr[d0] = *reinterpret_cast<const bf16x8*>(qp + d0 * 16); }
;     ATT_DMA(t_begin, 0);
;     asm volatile("" :: "v"(qr[0]), "v"(qr[1]), "v"(qr[2]), "v"(qr[3]));
;     const int nt_ = t_end - t_begin; if (nt_ > 1) ATT_DMA(t_begin + 1, SLOTB); if (nt_ > 2) ATT_DMA(t_begin + 2, 2 * SLOTB);
;     f32x16 o[2]; o[0] = f32x16{}; o[1] = f32x16{}; float l_reg = 0.f;
;     if (nt_ > 2) ATT_WAIT_BAR(4); else if (nt_ > 1) ATT_WAIT_BAR(2); else ATT_WAIT_BAR(0);
; __device__ __forceinline__ void attn_phase(Frame& F, const AttnBufs& A) {
;     ...
;     for (int k = 0; k < 9; ++k) { const int idx = r + 32 * k, h6 = idx / 48, rest = idx % 48, br = rest >> 4, i16 = rest & 15;
;         const int rr = (br == 0) ? 0 : (br == 1 ? (i16 >> 2) : i16), c = (br == 0) ? i16 : (br == 1 ? (i16 & 3) : 0);
.LBB0_389:
	s_add_i32 s78, s74, 1
	s_cmp_lt_u32 s78, 9
	s_cbranch_scc0 .Ldil_pf_skip
	s_mov_b32 s101, m0
	s_lshl_b32 s78, s78, 5
	v_readlane_b32 s79, v254, 30
	s_or_b32 s78, s78, s79
	s_mul_hi_u32 s79, s78, 0xaaaaaaab
	s_lshr_b32 s79, s79, 5
	s_mul_i32 s80, s79, 48
	s_sub_i32 s78, s78, s80
	s_lshr_b32 s80, s78, 4
	s_and_b32 s81, s78, 15
	s_bfe_u32 s82, s78, 0x20002
	s_and_b32 s83, s78, 3
	s_cmp_eq_u32 s80, 1
	s_cselect_b32 s82, s82, s81
	s_cselect_b32 s83, s83, 0
	s_cselect_b32 s84, 2, 4
	s_cmp_lt_u32 s78, 16
	s_cselect_b32 s82, 0, s82
	s_cselect_b32 s83, s81, s83
	s_cselect_b32 s84, 0, s84
	s_lshl_b32 s85, s83, 8
	s_cmp_eq_u32 s83, 0
	s_cselect_b32 s83, 2, 0
	v_readlane_b32 s88, v254, 38
	v_readlane_b32 s89, v254, 39
	s_or_b32 s88, s88, s82
	v_readlane_b32 s82, v254, 48
	s_add_i32 s80, s85, s82
	s_ashr_i32 s81, s80, 31
	s_lshl_b64 s[80:81], s[80:81], s84
	s_add_u32 s80, s80, s88
	s_addc_u32 s81, s81, s89
	s_lshl_b64 s[80:81], s[80:81], 11
	v_readlane_b32 s82, v254, 42
	s_add_u32 s80, s82, s80
	v_readlane_b32 s82, v254, 45
	s_addc_u32 s81, s82, s81
	s_lshl_b32 s79, s79, 7
	s_add_u32 s80, s80, s79
	s_addc_u32 s81, s81, 0
	s_add_i32 s78, s84, 10
	v_lshlrev_b64 v[158:159], s78, v[146:147]
	v_lshl_add_u64 v[158:159], v[158:159], 1, s[80:81]
	v_mov_b32_e32 v160, v148
	v_mov_b32_e32 v161, 0
	v_lshl_add_u64 v[158:159], v[158:159], 0, v[160:161]
	global_load_dwordx4 v[98:101], v[158:159], off offset:1280
	global_load_dwordx4 v[102:105], v[158:159], off offset:1312
	global_load_dwordx4 v[106:109], v[158:159], off offset:1344
	global_load_dwordx4 v[110:113], v[158:159], off offset:1376
	s_add_i32 s80, s85, 0xffffff80
	s_ashr_i32 s81, s80, 31
	s_lshl_b64 s[80:81], s[80:81], s84
	s_add_u32 s80, s80, s88
	s_addc_u32 s81, s81, s89
	s_lshl_b64 s[80:81], s[80:81], 11
	v_readlane_b32 s82, v254, 49
	s_add_u32 s88, s82, s80
	v_readlane_b32 s82, v254, 50
	s_addc_u32 s89, s82, s81
	s_add_u32 s88, s88, s79
	s_addc_u32 s89, s89, 0
	v_readlane_b32 s82, v254, 53
	s_add_u32 s80, s82, s80
	v_readlane_b32 s82, v254, 54
	s_addc_u32 s81, s82, s81
	s_add_u32 s80, s80, s79
	s_addc_u32 s81, s81, 0
	v_lshlrev_b64 v[162:163], s78, v[194:195]
	v_lshl_add_u64 v[162:163], v[162:163], 1, s[88:89]
	s_lshl_b32 s88, s76, 3
	s_mov_b32 s89, 0
	v_lshl_add_u64 v[162:163], s[88:89], 1, v[162:163]
	s_lshl_b32 s82, s76, 4
	s_and_b32 s82, s82, 48
	v_or_b32_e32 v164, s82, v178
	v_mov_b32_e32 v165, 0
	v_lshlrev_b64 v[164:165], s78, v[164:165]
	v_lshl_add_u64 v[164:165], v[164:165], 1, s[80:81]
	s_ashr_i32 s88, s77, 3
	s_and_b32 s88, s88, 0xffffffe0
	v_lshl_add_u64 v[164:165], s[88:89], 1, v[164:165]
	v_mov_b32_e32 v160, v150
	v_lshl_add_u64 v[164:165], v[164:165], 0, v[160:161]
	s_add_i32 s78, s84, 17
	s_mov_b32 s81, 0
	s_mov_b32 s80, s83
	s_lshl_b64 s[80:81], s[80:81], s78
	s_add_u32 s80, s80, 0x500
	s_addc_u32 s81, s81, 0
	s_lshl_b32 s82, s76, 10
	v_lshl_add_u64 v[166:167], v[162:163], 0, s[80:81]
	v_lshl_add_u64 v[168:169], v[164:165], 0, s[80:81]
	s_mov_b32 m0, s82
	s_add_i32 s85, s82, 0x8000
	global_load_lds_dwordx4 v[166:167], off
	s_mov_b32 m0, s85
	s_mov_b32 s88, 1
	s_lshl_b64 s[88:89], s[88:89], s78
	global_load_lds_dwordx4 v[168:169], off
	v_lshl_add_u64 v[166:167], v[166:167], 0, s[88:89]
	v_lshl_add_u64 v[168:169], v[168:169], 0, s[88:89]
	s_add_i32 m0, s82, 0x2000
	s_nop 0
	global_load_lds_dwordx4 v[166:167], off
	s_add_i32 m0, s85, 0x2000
	s_nop 0
	global_load_lds_dwordx4 v[168:169], off
	v_lshl_add_u64 v[166:167], v[166:167], 0, s[88:89]
	v_lshl_add_u64 v[168:169], v[168:169], 0, s[88:89]
	s_add_i32 m0, s82, 0x4000
	s_nop 0
	global_load_lds_dwordx4 v[166:167], off
	s_add_i32 m0, s85, 0x4000
	s_nop 0
	global_load_lds_dwordx4 v[168:169], off
	s_mov_b32 m0, s101

; __global__ void __launch_bounds__(NWAVES * 64, 2) mk_fwd(Args args) {
	.amdhsa_kernel _Z6mk_fwd4Args
		.amdhsa_group_segment_fixed_size 147456
		.amdhsa_private_segment_fixed_size 0
		.amdhsa_kernarg_size 368
		.amdhsa_user_sgpr_count 2
		.amdhsa_user_sgpr_dispatch_ptr 0
		.amdhsa_user_sgpr_queue_ptr 0
		.amdhsa_user_sgpr_kernarg_segment_ptr 1
		.amdhsa_user_sgpr_dispatch_id 0
		.amdhsa_user_sgpr_kernarg_preload_length 0
		.amdhsa_user_sgpr_kernarg_preload_offset 0
		.amdhsa_user_sgpr_private_segment_size 0
		.amdhsa_uses_dynamic_stack 0
		.amdhsa_enable_private_segment 0
		.amdhsa_system_sgpr_workgroup_id_x 1
		.amdhsa_system_sgpr_workgroup_id_y 0
		.amdhsa_system_sgpr_workgroup_id_z 0
		.amdhsa_system_sgpr_workgroup_info 0
		.amdhsa_system_vgpr_workitem_id 0
		.amdhsa_next_free_vgpr 256
		.amdhsa_next_free_sgpr 102
		.amdhsa_accum_offset 256
		.amdhsa_reserve_vcc 1
		.amdhsa_float_round_mode_32 0
		.amdhsa_float_round_mode_16_64 0
		.amdhsa_float_denorm_mode_32 3
		.amdhsa_float_denorm_mode_16_64 3
		.amdhsa_dx10_clamp 1
		.amdhsa_ieee_mode 1
		.amdhsa_fp16_overflow 0
		.amdhsa_tg_split 0
		.amdhsa_exception_fp_ieee_invalid_op 0
		.amdhsa_exception_fp_denorm_src 0
		.amdhsa_exception_fp_ieee_div_zero 0
		.amdhsa_exception_fp_ieee_overflow 0
		.amdhsa_exception_fp_ieee_underflow 0
		.amdhsa_exception_fp_ieee_inexact 0
		.amdhsa_exception_int_div_zero 0
	.end_amdhsa_kernel

; __global__ void __launch_bounds__(NWAVES * 64, 2) mk_fwd(Args args) {
amdhsa.kernels:
  - .agpr_count:     0
    .args:
      - .offset:         0
        .size:           112
        .value_kind:     by_value
      - .offset:         112
        .size:           4
        .value_kind:     hidden_block_count_x
      - .offset:         116
        .size:           4
        .value_kind:     hidden_block_count_y
      - .offset:         120
        .size:           4
        .value_kind:     hidden_block_count_z
      - .offset:         124
        .size:           2
        .value_kind:     hidden_group_size_x
      - .offset:         126
        .size:           2
        .value_kind:     hidden_group_size_y
      - .offset:         128
        .size:           2
        .value_kind:     hidden_group_size_z
      - .offset:         130
        .size:           2
        .value_kind:     hidden_remainder_x
      - .offset:         132
        .size:           2
        .value_kind:     hidden_remainder_y
      - .offset:         134
        .size:           2
        .value_kind:     hidden_remainder_z
      - .offset:         152
        .size:           8
        .value_kind:     hidden_global_offset_x
      - .offset:         160
        .size:           8
        .value_kind:     hidden_global_offset_y
      - .offset:         168
        .size:           8
        .value_kind:     hidden_global_offset_z
      - .offset:         176
        .size:           2
        .value_kind:     hidden_grid_dims
    .group_segment_fixed_size: 147456
    .kernarg_segment_align: 8
    .kernarg_segment_size: 368
    .language:       OpenCL C
    .language_version:
      - 2
      - 0
    .max_flat_workgroup_size: 512
    .name:           _Z6mk_fwd4Args
    .private_segment_fixed_size: 0
    .sgpr_count:     108
    .sgpr_spill_count: 240
    .symbol:         _Z6mk_fwd4Args.kd
    .uniform_work_group_size: 1
    .uses_dynamic_stack: false
    .vgpr_count:     256
    .vgpr_spill_count: 0
    .wavefront_size: 64
